# final_kernel: fixed-point conversion via fma(val, scale, 1.5*2^52) + integer fixup (3 VALU per record instead of 8), same integers
# speedup vs baseline: 1.0081x; 1.0081x over previous
.LBB2_39:
	s_or_b64 exec, exec, s[20:21]
	v_mov_b32_e32 v0, 0
	s_waitcnt lgkmcnt(0)
	s_barrier
	ds_read_b32 v0, v0 offset:1568
	s_waitcnt lgkmcnt(0)
	v_bfe_u32 v5, v0, 23, 8
	v_sub_u32_e32 v0, 0xa5, v5
	v_ldexp_f64 v[0:1], 1.0, v0
	s_mov_b32 s36, 0
	s_mov_b32 s37, 0x43380000
	s_and_saveexec_b64 s[0:1], s[16:17]
	s_cbranch_execnz .LBB2_48
	s_or_b64 exec, exec, s[0:1]
	s_and_saveexec_b64 s[0:1], s[14:15]
	s_cbranch_execnz .LBB2_49

.LBB2_48:
	v_cvt_f64_f32_e32 v[28:29], v26
	v_fma_f64 v[28:29], v[28:29], v[0:1], s[36:37]
	v_ashrrev_i32_e32 v3, 19, v14
	v_add_u32_e32 v29, 0xbcc80000, v29
	v_lshlrev_b32_e32 v3, 3, v3
	ds_add_u64 v3, v[28:29]
	s_or_b64 exec, exec, s[0:1]
	s_and_saveexec_b64 s[0:1], s[14:15]
	s_cbranch_execz .LBB2_41
.LBB2_49:
	v_cvt_f64_f32_e32 v[26:27], v27
	v_fma_f64 v[26:27], v[26:27], v[0:1], s[36:37]
	v_ashrrev_i32_e32 v3, 19, v16
	v_add_u32_e32 v27, 0xbcc80000, v27
	v_lshlrev_b32_e32 v3, 3, v3
	ds_add_u64 v3, v[26:27]
	s_or_b64 exec, exec, s[0:1]
	s_and_saveexec_b64 s[0:1], s[12:13]
	s_cbranch_execz .LBB2_42
.LBB2_50:
	v_cvt_f64_f32_e32 v[16:17], v17
	v_fma_f64 v[16:17], v[16:17], v[0:1], s[36:37]
	v_ashrrev_i32_e32 v3, 19, v10
	v_add_u32_e32 v17, 0xbcc80000, v17
	v_lshlrev_b32_e32 v3, 3, v3
	ds_add_u64 v3, v[16:17]
	s_or_b64 exec, exec, s[0:1]
	s_and_saveexec_b64 s[0:1], s[10:11]
	s_cbranch_execz .LBB2_43
.LBB2_51:
	v_cvt_f64_f32_e32 v[14:15], v15
	v_fma_f64 v[14:15], v[14:15], v[0:1], s[36:37]
	v_ashrrev_i32_e32 v3, 19, v12
	v_add_u32_e32 v15, 0xbcc80000, v15
	v_lshlrev_b32_e32 v3, 3, v3
	ds_add_u64 v3, v[14:15]
	s_or_b64 exec, exec, s[0:1]
	s_and_saveexec_b64 s[0:1], s[8:9]
	s_cbranch_execz .LBB2_44
.LBB2_52:
	v_cvt_f64_f32_e32 v[12:13], v13
	v_fma_f64 v[12:13], v[12:13], v[0:1], s[36:37]
	v_ashrrev_i32_e32 v3, 19, v6
	v_add_u32_e32 v13, 0xbcc80000, v13
	v_lshlrev_b32_e32 v3, 3, v3
	ds_add_u64 v3, v[12:13]
	s_or_b64 exec, exec, s[0:1]
	s_and_saveexec_b64 s[0:1], s[6:7]
	s_cbranch_execz .LBB2_45
.LBB2_53:
	v_cvt_f64_f32_e32 v[10:11], v11
	v_fma_f64 v[10:11], v[10:11], v[0:1], s[36:37]
	v_ashrrev_i32_e32 v3, 19, v8
	v_add_u32_e32 v11, 0xbcc80000, v11
	v_lshlrev_b32_e32 v3, 3, v3
	ds_add_u64 v3, v[10:11]
	s_or_b64 exec, exec, s[0:1]
	s_and_saveexec_b64 s[0:1], s[4:5]
	s_cbranch_execz .LBB2_46
.LBB2_54:
	v_cvt_f64_f32_e32 v[8:9], v9
	v_fma_f64 v[8:9], v[8:9], v[0:1], s[36:37]
	v_ashrrev_i32_e32 v2, 19, v2
	v_add_u32_e32 v9, 0xbcc80000, v9
	v_lshlrev_b32_e32 v2, 3, v2
	ds_add_u64 v2, v[8:9]
	s_or_b64 exec, exec, s[0:1]
	s_and_saveexec_b64 s[0:1], vcc
	s_cbranch_execz .LBB2_47
.LBB2_55:
	v_cvt_f64_f32_e32 v[2:3], v7
	v_fma_f64 v[2:3], v[2:3], v[0:1], s[36:37]
	v_ashrrev_i32_e32 v4, 19, v4
	v_add_u32_e32 v3, 0xbcc80000, v3
	v_lshlrev_b32_e32 v4, 3, v4
	ds_add_u64 v4, v[2:3]
	s_or_b64 exec, exec, s[0:1]
	s_and_saveexec_b64 s[0:1], s[2:3]
	s_cbranch_execz .LBB2_58

.LBB2_57:
	global_load_dwordx2 v[6:7], v[2:3], off
	v_add_u32_e32 v24, 4, v24
	v_cmp_ge_i32_e32 vcc, v24, v35
	s_or_b64 s[2:3], vcc, s[2:3]
	v_lshl_add_u64 v[2:3], v[2:3], 0, 32
	s_waitcnt vmcnt(0)
	v_and_b32_e32 v4, 0x7ffff, v6
	v_lshlrev_b32_e32 v4, 2, v4
	global_load_dword v4, v4, s[24:25]
	v_ashrrev_i32_e32 v6, 19, v6
	v_lshlrev_b32_e32 v10, 3, v6
	s_waitcnt vmcnt(0)
	v_mul_f32_e32 v4, v7, v4
	v_cvt_f64_f32_e32 v[8:9], v4
	v_fma_f64 v[8:9], v[8:9], v[0:1], s[36:37]
	s_nop 0
	v_add_u32_e32 v9, 0xbcc80000, v9
	ds_add_u64 v10, v[8:9]
	s_andn2_b64 exec, exec, s[2:3]
	s_cbranch_execnz .LBB2_57
